# RWKV and mLSTM chunk loops: next-chunk global prefetch issued after the wave-group barrier arrive instead of before it
# speedup vs baseline: 1.0014x; 1.0014x over previous
; #define LAS __attribute__((address_space(3)))
; #define LDS_WAIT() asm volatile("s_waitcnt lgkmcnt(0)" ::: "memory")
; __device__ __forceinline__ unsigned pk2(float lo, float hi) { const f32x2 v = {lo, hi}; const bf16x2_t b = __builtin_convertvector(v, bf16x2_t); return __builtin_bit_cast(unsigned, b); }
; __device__ __forceinline__ void mlstm_scan_unit(Frame& F, int unit, LAS unsigned* bcnt, unsigned& btarget) {
;     ...
;         for (int i = 0; i < 4; ++i) { *(LAS v4u*)(Lq + (pr0 + 16 * i) * 136 + pc) = rq[i]; *(LAS v4u*)(Lk + (pr0 + 16 * i) * 136 + pc) = rk[i]; }
;         LDS_WAIT();
;         { const int j = tid >> 2, d0 = 8 * (tid & 3); const float wkj = swk[j]; *(LAS v4u*)(Lv + j * VS + d0) = rv;
;           const unsigned uu[4] = {rv.x, rv.y, rv.z, rv.w}; v4u sv;
;           sv.x = pk2(wkj * __uint_as_float(uu[0] << 16), wkj * __uint_as_float(uu[0] & 0xffff0000u)); sv.y = pk2(wkj * __uint_as_float(uu[1] << 16), wkj * __uint_as_float(uu[1] & 0xffff0000u));
;           sv.z = pk2(wkj * __uint_as_float(uu[2] << 16), wkj * __uint_as_float(uu[2] & 0xffff0000u)); sv.w = pk2(wkj * __uint_as_float(uu[3] << 16), wkj * __uint_as_float(uu[3] & 0xffff0000u));
;           *(LAS v4u*)(Lvs + j * VS + d0) = sv; }
;         if (ch + 1 < SEQ / 64) ML_LOAD(ch + 1);
;         rw_bar(bcnt, btarget, lane);
.LBB0_925:
	ds_write_b128 v113, v[2:5] offset:45056
	ds_write_b128 v113, v[6:9] offset:62464
	ds_write_b128 v113, v[10:13] offset:49408
	ds_write_b128 v114, v[14:17] offset:4352
	ds_write_b128 v113, v[18:21] offset:53760
	ds_write_b128 v114, v[22:25] offset:8704
	ds_write_b128 v113, v[26:29] offset:58112
	ds_write_b128 v114, v[30:33] offset:13056
	s_waitcnt lgkmcnt(0)
	ds_read_b32 v72, v105
	v_lshlrev_b32_e32 v68, 16, v34
	v_and_b32_e32 v69, 0xffff0000, v34
	v_lshlrev_b32_e32 v70, 16, v35
	v_and_b32_e32 v71, 0xffff0000, v35
	s_waitcnt lgkmcnt(0)
	v_pk_mul_f32 v[68:69], v[72:73], v[68:69] op_sel_hi:[0,1]
	v_pk_mul_f32 v[70:71], v[72:73], v[70:71] op_sel_hi:[0,1]
	v_cvt_pk_bf16_f32 v68, v68, v69
	v_cvt_pk_bf16_f32 v69, v70, v71
	v_lshlrev_b32_e32 v70, 16, v36
	v_and_b32_e32 v71, 0xffff0000, v36
	v_lshlrev_b32_e32 v74, 16, v37
	v_and_b32_e32 v75, 0xffff0000, v37
	s_add_i32 s70, s71, 1
	v_pk_mul_f32 v[70:71], v[72:73], v[70:71] op_sel_hi:[0,1]
	v_pk_mul_f32 v[72:73], v[72:73], v[74:75] op_sel_hi:[0,1]
	v_cvt_pk_bf16_f32 v70, v70, v71
	v_cvt_pk_bf16_f32 v71, v72, v73
	s_cmp_eq_u32 s71, 31
	ds_write_b128 v106, v[34:37]
	ds_write_b128 v107, v[68:71]
.LBB0_927:
	s_and_saveexec_b64 s[58:59], s[4:5]
	s_cbranch_execz .LBB0_930
	s_mov_b64 s[60:61], exec
	v_mbcnt_lo_u32_b32 v41, s60, 0
	v_mbcnt_hi_u32_b32 v41, s61, v41
	v_cmp_eq_u32_e32 vcc, 0, v41
	s_and_b64 s[62:63], exec, vcc
	s_mov_b64 exec, s[62:63]
	s_bcnt1_i32_b64 s0, s[60:61]
	v_mov_b32_e32 v41, s67
	v_mov_b32_e32 v67, s0
	s_waitcnt lgkmcnt(0)
	ds_add_u32 v41, v67
.LBB0_930:
	s_or_b64 exec, exec, s[58:59]
	s_cmp_eq_u32 s71, 31
	s_cbranch_scc1 .Lml_pf_skip
	s_lshl_b32 s0, s70, 6
	s_add_u32 s58, s50, s0
	s_addc_u32 s59, s51, 0
	v_lshl_add_u64 v[2:3], s[58:59], 0, v[80:81]
	v_lshlrev_b64 v[2:3], 11, v[2:3]
	v_lshl_add_u64 v[26:27], v[94:95], 0, v[2:3]
	v_add_co_u32_e32 v14, vcc, 0x8000, v26
	v_lshl_add_u64 v[34:35], s[58:59], 0, v[86:87]
	v_mov_b64_e32 v[36:37], s[2:3]
	v_addc_co_u32_e32 v15, vcc, 0, v27, vcc
	v_mad_u64_u32 v[36:37], s[60:61], v34, s66, v[36:37]
	v_add_co_u32_e32 v22, vcc, 0x10000, v26
	v_mad_i32_i24 v37, v35, s66, v37
	s_lshl_b32 s0, s52, 1
	v_addc_co_u32_e32 v23, vcc, 0, v27, vcc
	v_lshl_add_u64 v[34:35], v[36:37], 0, s[0:1]
	s_mov_b32 s55, s1
	v_add_co_u32_e32 v30, vcc, 0x18000, v26
	v_lshl_add_u64 v[34:35], v[34:35], 0, s[54:55]
	s_nop 0
	v_addc_co_u32_e32 v31, vcc, 0, v27, vcc
	v_lshl_add_u64 v[34:35], v[34:35], 0, v[82:83]
	v_mov_b32_e32 v37, s59
	v_or_b32_e32 v36, s58, v162
	v_add_co_u32_e32 v34, vcc, 0x2000, v34
	v_lshlrev_b64 v[36:37], 6, v[36:37]
	s_nop 0
	v_addc_co_u32_e32 v35, vcc, 0, v35, vcc
	v_lshl_add_u64 v[38:39], s[56:57], 0, v[36:37]
	global_load_dwordx4 v[2:5], v[26:27], off
	global_load_dwordx4 v[6:9], v[26:27], off offset:1024
	global_load_dwordx4 v[10:13], v[14:15], off
	s_nop 0
	global_load_dwordx4 v[14:17], v[14:15], off offset:1024
	s_nop 0
	global_load_dwordx4 v[18:21], v[22:23], off
	s_nop 0
	global_load_dwordx4 v[22:25], v[22:23], off offset:1024
	s_nop 0
	global_load_dwordx4 v[26:29], v[30:31], off
	s_nop 0
	global_load_dwordx4 v[30:33], v[30:31], off offset:1024
	s_nop 0
	global_load_dwordx4 v[34:37], v[34:35], off offset:896
	s_nop 0
	global_load_dwordx4 v[244:247], v[38:39], off
.Lml_pf_skip:
	s_add_i32 s0, s53, 4
	s_branch .LBB0_932

; #define LAS __attribute__((address_space(3)))
; __device__ __forceinline__ void rwkv_chunk_unit(Frame& F, int unit, LAS unsigned char* regB, LAS unsigned* bcnt, unsigned& btarget) {
;     ...
;         { const int tq = lane & 31, hq = lane >> 5; f32x4 c0v, c1v;
; #pragma unroll
;           for (int j = 0; j < 4; ++j) { c0v[j] = scan32(ws0[j]); c1v[j] = scan32(ws1[j]); }
;           *(LAS f32x4*)(csf + tq * 64 + 16 * w + 8 * hq) = c0v; *(LAS f32x4*)(csf + tq * 64 + 16 * w + 8 * hq + 4) = c1v; }
;         if (ch + 1 < SEQ / 32) RC_LOAD(ch + 1);
;         rw_bar(bcnt, btarget, lane);
.LBB0_994:
	s_or_b64 exec, exec, s[4:5]
	s_waitcnt vmcnt(2)
	v_mov_b32_dpp v2, v86 row_shr:1 row_mask:0xf bank_mask:0xf bound_ctrl:1
	v_mov_b32_dpp v3, v87 row_shr:1 row_mask:0xf bank_mask:0xf bound_ctrl:1
	v_mov_b32_dpp v4, v82 row_shr:1 row_mask:0xf bank_mask:0xf bound_ctrl:1
	v_pk_add_f32 v[2:3], v[86:87], v[2:3]
	v_mov_b32_dpp v5, v83 row_shr:1 row_mask:0xf bank_mask:0xf bound_ctrl:1
	v_pk_add_f32 v[4:5], v[82:83], v[4:5]
	v_mov_b32_dpp v6, v2 row_shr:2 row_mask:0xf bank_mask:0xf bound_ctrl:1
	v_mov_b32_dpp v7, v3 row_shr:2 row_mask:0xf bank_mask:0xf bound_ctrl:1
	v_pk_add_f32 v[2:3], v[2:3], v[6:7]
	v_mov_b32_dpp v8, v4 row_shr:2 row_mask:0xf bank_mask:0xf bound_ctrl:1
	v_mov_b32_dpp v9, v5 row_shr:2 row_mask:0xf bank_mask:0xf bound_ctrl:1
	v_mov_b32_dpp v6, v2 row_shr:4 row_mask:0xf bank_mask:0xf bound_ctrl:1
	v_mov_b32_dpp v7, v3 row_shr:4 row_mask:0xf bank_mask:0xf bound_ctrl:1
	v_pk_add_f32 v[4:5], v[4:5], v[8:9]
	v_pk_add_f32 v[2:3], v[2:3], v[6:7]
	v_mov_b32_e32 v196, 0
	v_mov_b32_dpp v8, v4 row_shr:4 row_mask:0xf bank_mask:0xf bound_ctrl:1
	v_mov_b32_dpp v9, v5 row_shr:4 row_mask:0xf bank_mask:0xf bound_ctrl:1
	v_mov_b32_dpp v6, v2 row_shr:8 row_mask:0xf bank_mask:0xf bound_ctrl:1
	v_mov_b32_dpp v7, v3 row_shr:8 row_mask:0xf bank_mask:0xf bound_ctrl:1
	v_pk_add_f32 v[4:5], v[4:5], v[8:9]
	v_pk_add_f32 v[2:3], v[2:3], v[6:7]
	v_mov_b32_e32 v6, 0
	v_mov_b32_e32 v7, 0
	v_mov_b32_dpp v8, v4 row_shr:8 row_mask:0xf bank_mask:0xf bound_ctrl:1
	v_mov_b32_dpp v9, v5 row_shr:8 row_mask:0xf bank_mask:0xf bound_ctrl:1
	v_mov_b32_dpp v6, v2 row_bcast:15 row_mask:0xa bank_mask:0xf
	v_mov_b32_dpp v7, v3 row_bcast:15 row_mask:0xa bank_mask:0xf
	v_pk_add_f32 v[10:11], v[4:5], v[8:9]
	v_mov_b32_dpp v4, v88 row_shr:1 row_mask:0xf bank_mask:0xf bound_ctrl:1
	v_mov_b32_dpp v8, v84 row_shr:1 row_mask:0xf bank_mask:0xf bound_ctrl:1
	v_mov_b32_dpp v5, v89 row_shr:1 row_mask:0xf bank_mask:0xf bound_ctrl:1
	v_mov_b32_dpp v9, v85 row_shr:1 row_mask:0xf bank_mask:0xf bound_ctrl:1
	v_pk_add_f32 v[4:5], v[88:89], v[4:5]
	v_pk_add_f32 v[2:3], v[2:3], v[6:7]
	v_pk_add_f32 v[6:7], v[84:85], v[8:9]
	v_mov_b32_dpp v198, v4 row_shr:2 row_mask:0xf bank_mask:0xf bound_ctrl:1
	v_mov_b32_dpp v199, v5 row_shr:2 row_mask:0xf bank_mask:0xf bound_ctrl:1
	v_mov_b32_dpp v8, v6 row_shr:2 row_mask:0xf bank_mask:0xf bound_ctrl:1
	v_mov_b32_dpp v9, v7 row_shr:2 row_mask:0xf bank_mask:0xf bound_ctrl:1
	v_pk_add_f32 v[4:5], v[4:5], v[198:199]
	v_pk_add_f32 v[6:7], v[6:7], v[8:9]
	v_mov_b32_e32 v197, 0
	v_mov_b32_dpp v198, v4 row_shr:4 row_mask:0xf bank_mask:0xf bound_ctrl:1
	v_mov_b32_dpp v199, v5 row_shr:4 row_mask:0xf bank_mask:0xf bound_ctrl:1
	v_mov_b32_dpp v8, v6 row_shr:4 row_mask:0xf bank_mask:0xf bound_ctrl:1
	v_mov_b32_dpp v9, v7 row_shr:4 row_mask:0xf bank_mask:0xf bound_ctrl:1
	v_pk_add_f32 v[4:5], v[4:5], v[198:199]
	v_pk_add_f32 v[6:7], v[6:7], v[8:9]
	v_mov_b32_dpp v196, v10 row_bcast:15 row_mask:0xa bank_mask:0xf
	v_mov_b32_dpp v198, v4 row_shr:8 row_mask:0xf bank_mask:0xf bound_ctrl:1
	v_mov_b32_dpp v199, v5 row_shr:8 row_mask:0xf bank_mask:0xf bound_ctrl:1
	v_mov_b32_dpp v8, v6 row_shr:8 row_mask:0xf bank_mask:0xf bound_ctrl:1
	v_mov_b32_dpp v9, v7 row_shr:8 row_mask:0xf bank_mask:0xf bound_ctrl:1
	v_pk_add_f32 v[4:5], v[4:5], v[198:199]
	v_mov_b32_e32 v198, 0
	v_mov_b32_e32 v199, 0
	v_pk_add_f32 v[6:7], v[6:7], v[8:9]
	v_mov_b32_e32 v8, 0
	v_mov_b32_e32 v9, 0
	v_mov_b32_dpp v197, v11 row_bcast:15 row_mask:0xa bank_mask:0xf
	v_mov_b32_dpp v198, v4 row_bcast:15 row_mask:0xa bank_mask:0xf
	v_mov_b32_dpp v199, v5 row_bcast:15 row_mask:0xa bank_mask:0xf
	v_mov_b32_dpp v8, v6 row_bcast:15 row_mask:0xa bank_mask:0xf
	v_mov_b32_dpp v9, v7 row_bcast:15 row_mask:0xa bank_mask:0xf
	s_add_i32 s18, s10, 1
	v_pk_add_f32 v[4:5], v[4:5], v[198:199]
	v_pk_add_f32 v[8:9], v[6:7], v[8:9]
	v_pk_add_f32 v[6:7], v[10:11], v[196:197]
	s_cmp_eq_u32 s10, 63
	ds_write_b128 v99, v[2:5]
	ds_write_b128 v99, v[6:9] offset:16
.LBB0_996:
	s_and_saveexec_b64 s[4:5], s[6:7]
	s_cbranch_execz .LBB0_999
	s_mov_b64 s[96:97], exec
	v_mbcnt_lo_u32_b32 v2, s96, 0
	v_mbcnt_hi_u32_b32 v2, s97, v2
	v_cmp_eq_u32_e32 vcc, 0, v2
	s_and_b64 s[10:11], exec, vcc
	s_mov_b64 exec, s[10:11]
	s_bcnt1_i32_b64 s10, s[96:97]
	v_mov_b32_e32 v2, s12
	v_mov_b32_e32 v3, s10
	s_waitcnt lgkmcnt(0)
	ds_add_u32 v2, v3
.LBB0_999:
	s_or_b64 exec, exec, s[4:5]
	s_cmp_eq_u32 s18, 64
	s_cbranch_scc1 .Lrw_pf_skip
	s_lshl_b32 s96, s18, 5
	v_or_b32_e32 v96, s96, v94
	v_lshl_add_u64 v[2:3], s[94:95], 0, v[96:97]
	v_mad_u64_u32 v[4:5], s[4:5], v2, s33, v[124:125]
	v_mad_i32_i24 v5, v3, s33, v5
	v_add_co_u32_e32 v6, vcc, 0x1000, v4
	global_load_dwordx2 v[128:129], v[4:5], off
	global_load_dwordx2 v[130:131], v[4:5], off offset:2048
	v_addc_co_u32_e32 v7, vcc, 0, v5, vcc
	global_load_dwordx2 v[132:133], v[6:7], off
	v_add_co_u32_e32 v6, vcc, 0xffffb000, v4
	v_lshlrev_b64 v[2:3], 12, v[2:3]
	s_nop 0
	v_addc_co_u32_e32 v7, vcc, -1, v5, vcc
	v_add_co_u32_e32 v4, vcc, 0xffffc000, v4
	v_lshl_add_u64 v[2:3], v[134:135], 0, v[2:3]
	s_nop 0
	v_addc_co_u32_e32 v5, vcc, -1, v5, vcc
	global_load_dwordx2 v[136:137], v[6:7], off offset:-1024
	global_load_dwordx2 v[140:141], v[4:5], off offset:-3072
	global_load_dwordx2 v[138:139], v[4:5], off offset:-1024
	v_add_u32_e32 v96, 16, v96
	global_load_dwordx2 v[240:241], v[2:3], off
	s_mov_b32 s97, s1
	v_lshl_add_u64 v[2:3], s[94:95], 0, v[96:97]
	v_mad_u64_u32 v[4:5], s[4:5], v2, s33, v[124:125]
	s_movk_i32 s4, 0x1000
	v_mad_i32_i24 v5, v3, s33, v5
	v_add_co_u32_e32 v6, vcc, s4, v4
	s_movk_i32 s4, 0xb000
	s_nop 0
	v_addc_co_u32_e32 v7, vcc, 0, v5, vcc
	global_load_dwordx2 v[144:145], v[4:5], off
	global_load_dwordx2 v[146:147], v[4:5], off offset:2048
	global_load_dwordx2 v[148:149], v[6:7], off
	v_add_co_u32_e32 v6, vcc, s4, v4
	s_movk_i32 s4, 0xc000
	s_nop 0
	v_addc_co_u32_e32 v7, vcc, -1, v5, vcc
	v_add_co_u32_e32 v4, vcc, s4, v4
	v_lshlrev_b64 v[2:3], 12, v[2:3]
	s_nop 0
	v_addc_co_u32_e32 v5, vcc, -1, v5, vcc
	v_lshl_add_u64 v[2:3], v[134:135], 0, v[2:3]
	global_load_dwordx2 v[150:151], v[6:7], off offset:-1024
	global_load_dwordx2 v[154:155], v[4:5], off offset:-3072
	global_load_dwordx2 v[158:159], v[4:5], off offset:-1024
	s_nop 0
	global_load_dwordx2 v[242:243], v[2:3], off
	v_lshl_add_u64 v[2:3], v[142:143], 0, s[96:97]
	v_lshlrev_b64 v[2:3], 12, v[2:3]
	v_lshl_add_u64 v[2:3], v[156:157], 0, v[2:3]
	global_load_dwordx4 v[82:85], v[2:3], off offset:16
	global_load_dwordx4 v[86:89], v[2:3], off
.Lrw_pf_skip:
	s_add_i32 s10, s13, 4
	s_branch .LBB0_1001
